# phase-start de-serialisation in five GEMMs (in-proj, q up-proj, kv up-proj, out-proj, dense gate/up): row-statistics wait/compute/table write moved behind the first-tile LDS-DMA issue; stray mid-prolo
# speedup vs baseline: 1.0110x; 1.0068x over previous
; __device__ __forceinline__ int launder_v(int v) { asm volatile("" : "+v"(v)); return v; }
; __device__ __forceinline__ float rsq_(float x) { return 1.0f / sqrtf(x); }
; #define PG8_STAGEB(bufoff, gbase) do { _Pragma("unroll") for (int _i = 0; _i < 2; ++_i) PG8_GL((const char*)(gbase) + voffB[_i], bufoff, _i); } while (0)
; #define PG8_STAGEA(bufoff, ubase, offs, h, kb) do { _Pragma("unroll") for (int _i = 0; _i < 2; ++_i) { \
;         if constexpr (P::GATHER) PG8_GL(S.A + (size_t)(kb) + (offs)[h][_i], bufoff, _i); \
;         else PG8_GL((const char*)(ubase) + (size_t)(h) * hstepA + (size_t)(kb) + voffA[_i], bufoff, _i); } } while (0)
; #define PG8_WAIT_V(n) asm volatile("s_waitcnt vmcnt(" #n ")" ::: "memory")
; #define PG8_BAR __builtin_amdgcn_s_barrier()
; __device__ __forceinline__ LAS float* T0(ldsp tab, int par) { return (LAS float*)(tab) + par * 256; }
; #define PROB_WS() unsigned char* w_ = ws; asm volatile("" : "+s"(w_))
; template <class P, bool ALIGN_EPI>
; __device__ __forceinline__ void gemm_phase(ldsp lds, ldsp tab, const P& S) {
;     ...
;     S.prepare(cur, 0, tab);
;     PG8_STAGEB(PG8_SB(0, 0), cB); PG8_STAGEB(PG8_SB(0, 1), cB + hstepB); PG8_STAGEA(PG8_SA(0, 0), cA, goc, 0, 0); PG8_STAGEA(PG8_SA(0, 1), cA, goc, 1, 0);
;     if (wr == 1) PG8_BAR;
;     PG8_WAIT_V(2); PG8_BAR;
;     PG8_STAGEB(PG8_SB(1, 0), cB + kstep); PG8_STAGEA(PG8_SA(1, 0), cA, goc, 0, kstep); PG8_STAGEB(PG8_SB(1, 1), cB + hstepB + kstep);
;     PG8_WAIT_V(6); PG8_BAR;
;     __device__ __forceinline__ void prepare(const Unit& u, int par, ldsp tab) const {
;         PROB_WS(); const float* ssql = (const float*)(w_ + WS_SSQL);
;         const int tid = launder_v(threadIdx.x); if (tid < 256) { const int row = u.pm * 256 + tid; const f32x4 a = gld4(ssql + (size_t)row * 8); T0(tab, par)[tid] = rsq_(((a[0] + a[1]) + (a[2] + a[3])) * (1.0f / 256.0f) + EPS); } }
.LBB0_986:
	v_readlane_b32 s4, v253, 5
	s_cmp_le_i32 s4, s2
	s_cselect_b64 s[2:3], -1, 0
	s_and_b64 s[0:1], s[2:3], s[0:1]
	s_andn2_b64 vcc, exec, s[0:1]
	v_readlane_b32 s5, v253, 6
	s_cbranch_vccnz .LBB0_1074
	v_readlane_b32 s0, v253, 7
	v_readlane_b32 s2, v253, 9
	v_readlane_b32 s3, v253, 10
	s_mov_b64 s[4:5], s[2:3]
	v_readlane_b32 s29, v253, 3
	v_mov_b32_e32 v12, v0
	s_cmpk_gt_i32 s29, 0xbf
	v_readfirstlane_b32 s3, v12
	v_readlane_b32 s1, v253, 8
	s_cbranch_scc1 .LBB0_1011
	s_ashr_i32 s52, s29, 31
	s_lshr_b32 s0, s52, 29
	s_add_i32 s0, s29, s0
	s_ashr_i32 s1, s0, 3
	s_and_b32 s0, s0, -8
	s_sub_i32 s0, s29, s0
	s_cmp_lt_i32 s0, 0
	s_cselect_b32 s2, 25, 24
	s_mul_i32 s0, s0, s2
	s_add_i32 s0, s0, s1
	s_mul_hi_i32 s1, s0, 0x2aaaaaab
	s_lshr_b32 s2, s1, 31
	s_ashr_i32 s1, s1, 2
	s_add_i32 s1, s1, s2
	s_lshl_b32 s6, s1, 3
	s_mul_i32 s1, s1, 24
	s_sub_i32 s0, s0, s1
	s_bfe_i32 s1, s0, 0x80000
	s_bfe_u32 s1, s1, 0x3000c
	s_add_i32 s1, s0, s1
	s_bfe_i32 s2, s1, 0x80000
	s_and_b32 s1, s1, 0xf8
	s_sub_i32 s0, s0, s1
	s_sext_i32_i8 s0, s0
	s_sext_i32_i16 s2, s2
	s_add_i32 s20, s6, s0
	s_mov_b64 s[0:1], s[4:5]
	v_mov_b32_e32 v1, v0
	s_movk_i32 s6, 0x100
	s_lshr_b32 s2, s2, 3
	s_nop 0
	v_cmp_gt_i32_e32 vcc, s6, v1
	s_and_saveexec_b64 s[6:7], vcc
	s_cbranch_execz .LBB0_990
	s_waitcnt lgkmcnt(0)
	v_lshl_add_u32 v4, s20, 8, v1
	s_waitcnt lgkmcnt(0)
	v_ashrrev_i32_e32 v5, 31, v4
	v_lshlrev_b64 v[4:5], 5, v[4:5]
	v_lshl_add_u64 v[4:5], s[0:1], 0, v[4:5]
	v_add_co_u32_e32 v4, vcc, 0x464000, v4
	s_mov_b32 s0, 0xf800000
	s_nop 0
	v_addc_co_u32_e32 v5, vcc, 0, v5, vcc
	global_load_dwordx4 v[26:29], v[4:5], off
	v_lshl_add_u32 v31, v1, 2, 0
	v_add_u32_e32 v31, 0x20000, v31
.LBB0_990:
	s_or_b64 exec, exec, s[6:7]
	s_waitcnt lgkmcnt(0)
	v_bfe_i32 v4, v12, 27, 1
	v_lshlrev_b32_e32 v1, 4, v12
	v_lshrrev_b32_e32 v4, 22, v4
	s_mul_i32 s8, s26, 0x30000
	s_add_u32 s53, s4, 0x250f4000
	v_add_u32_e32 v4, v1, v4
	s_addc_u32 s54, s5, 0
	s_lshl_b64 s[0:1], s[8:9], 1
	v_and_b32_e32 v4, 0xfffffc00, v4
	s_add_u32 s0, s4, s0
	v_mov_b32_e32 v2, s2
	v_sub_u32_e32 v4, v1, v4
	s_addc_u32 s1, s5, s1
	v_readfirstlane_b32 s8, v2
	v_ashrrev_i32_e32 v2, 31, v12
	s_waitcnt lgkmcnt(0)
	v_lshrrev_b32_e32 v5, 4, v4
	s_add_u32 s55, s0, 0x1774000
	v_lshrrev_b32_e32 v2, 26, v2
	v_bitop3_b32 v4, v5, v4, 32 bitop3:0x6c
	s_addc_u32 s56, s1, 0
	s_ashr_i32 s21, s20, 31
	v_add_u32_e32 v2, v12, v2
	v_ashrrev_i32_e32 v6, 31, v4
	s_lshl_b64 s[0:1], s[20:21], 20
	v_ashrrev_i32_e32 v2, 6, v2
	v_lshrrev_b32_e32 v6, 26, v6
	s_add_u32 s0, s53, s0
	v_lshlrev_b32_e32 v5, 3, v2
	v_add_u32_e32 v6, v4, v6
	s_addc_u32 s1, s54, s1
	s_bfe_i64 s[6:7], s[8:9], 0x80000
	v_and_b32_e32 v5, -16, v5
	v_ashrrev_i32_e32 v7, 6, v6
	v_and_b32_e32 v6, 0xc0, v6
	s_lshl_b64 s[6:7], s[6:7], 17
	v_add_u32_e32 v5, v7, v5
	v_sub_u32_e32 v4, v4, v6
	s_add_u32 s22, s55, s6
	v_lshlrev_b32_e32 v2, 5, v2
	v_ashrrev_i16_sdwa v4, v248, sext(v4) dst_sel:DWORD dst_unused:UNUSED_PAD src0_sel:DWORD src1_sel:BYTE_0
	v_lshlrev_b32_e32 v6, 1, v5
	v_lshrrev_b32_e32 v8, 2, v5
	v_and_b32_e32 v7, 3, v7
	s_mov_b32 s6, 0x7fffe0
	v_and_b32_e32 v2, 32, v2
	v_bfe_i32 v4, v4, 0, 16
	v_and_b32_e32 v6, 24, v6
	v_and_b32_e32 v8, 4, v8
	v_and_or_b32 v7, v5, s6, v7
	v_or3_b32 v6, v7, v8, v6
	v_add_lshl_u32 v4, v2, v4, 1
	v_add_u32_e32 v1, 0x2000, v1
	v_lshl_add_u32 v2, v5, 12, v4
	v_lshl_add_u32 v196, v6, 9, v4
	v_ashrrev_i32_e32 v4, 31, v1
	v_lshrrev_b32_e32 v4, 22, v4
	v_add_u32_e32 v4, v1, v4
	v_ashrrev_i32_e32 v4, 10, v4
	v_mul_i32_i24_e32 v5, 0x400, v4
	v_sub_u32_e32 v1, v1, v5
	v_lshrrev_b32_e32 v5, 4, v1
	v_bitop3_b32 v1, v5, v1, 32 bitop3:0x6c
	v_ashrrev_i32_e32 v6, 31, v1
	v_lshrrev_b32_e32 v6, 26, v6
	v_lshlrev_b32_e32 v5, 3, v4
	v_add_u32_e32 v6, v1, v6
	s_addc_u32 s23, s56, s7
	s_ashr_i32 s10, s3, 6
	v_and_b32_e32 v5, -16, v5
	v_ashrrev_i32_e32 v7, 6, v6
	v_and_b32_e32 v6, 0xc0, v6
	v_add_u32_e32 v5, v7, v5
	v_sub_u32_e32 v1, v1, v6
	s_lshl_b32 s8, s10, 10
	v_lshlrev_b32_e32 v4, 5, v4
	v_ashrrev_i16_sdwa v1, v248, sext(v1) dst_sel:DWORD dst_unused:UNUSED_PAD src0_sel:DWORD src1_sel:BYTE_0
	v_lshlrev_b32_e32 v6, 1, v5
	v_lshrrev_b32_e32 v8, 2, v5
	v_and_b32_e32 v7, 3, v7
	s_add_i32 s57, s8, 0
	v_and_b32_e32 v4, 32, v4
	v_bfe_i32 v1, v1, 0, 16
	v_and_b32_e32 v6, 24, v6
	v_and_b32_e32 v8, 4, v8
	v_and_or_b32 v7, v5, s6, v7
	s_add_i32 m0, s57, 0x10000
	v_or3_b32 v6, v7, v8, v6
	v_add_lshl_u32 v1, v4, v1, 1
	s_ashr_i32 s11, s3, 8
	global_load_lds_dwordx4 v196, s[22:23]
	s_add_i32 m0, s57, 0x12000
	v_lshl_add_u32 v200, v6, 9, v1
	s_add_u32 s6, s22, 0x10000
	global_load_lds_dwordx4 v200, s[22:23]
	s_addc_u32 s7, s23, 0
	s_add_i32 m0, s57, 0x14000
	s_add_i32 s58, s57, 0x2000
	global_load_lds_dwordx4 v196, s[6:7]
	s_add_i32 m0, s57, 0x16000
	v_lshl_add_u32 v198, v5, 12, v1
	global_load_lds_dwordx4 v200, s[6:7]
	s_mov_b32 m0, s57
	s_add_u32 s6, s0, 0x80000
	global_load_lds_dwordx4 v2, s[0:1]
	s_mov_b32 m0, s58
	s_addc_u32 s7, s1, 0
	s_add_i32 s59, s57, 0x4000
	global_load_lds_dwordx4 v198, s[0:1]
	s_mov_b32 m0, s59
	s_add_i32 s60, s57, 0x6000
	global_load_lds_dwordx4 v2, s[6:7]
	s_mov_b32 m0, s60
	v_mov_b32_e32 v197, v3
	global_load_lds_dwordx4 v198, s[6:7]
	v_cmp_gt_i32_e32 vcc, 0x100, v0
	s_and_b64 exec, exec, vcc
	s_cbranch_execz .Lprep_pq_skip
	s_waitcnt vmcnt(8)
	v_mov_b32_e32 v8, v27
	v_mov_b32_e32 v9, v28
	v_mov_b32_e32 v4, v26
	v_mov_b32_e32 v5, v29
	v_pk_add_f32 v[4:5], v[8:9], v[4:5]
	s_nop 0
	v_add_f32_e32 v32, v4, v5
	v_fmamk_f32 v32, v32, 0x3b800000, v247
	v_mul_f32_e32 v4, 0x4f800000, v32
	v_cmp_gt_f32_e32 vcc, 0xf800000, v32
	s_nop 1
	v_cndmask_b32_e32 v32, v32, v4, vcc
	v_sqrt_f32_e32 v4, v32
	s_nop 0
	v_add_u32_e32 v5, -1, v4
	v_add_u32_e32 v6, 1, v4
	v_fma_f32 v7, -v5, v4, v32
	v_fma_f32 v8, -v6, v4, v32
	v_cmp_ge_f32_e64 s[6:7], 0, v7
	s_nop 1
	v_cndmask_b32_e64 v4, v4, v5, s[6:7]
	v_cmp_lt_f32_e64 s[6:7], 0, v8
	s_nop 1
	v_cndmask_b32_e64 v4, v4, v6, s[6:7]
	v_mul_f32_e32 v5, 0x37800000, v4
	v_cndmask_b32_e32 v4, v4, v5, vcc
	v_cmp_class_f32_e32 vcc, v32, v242
	s_nop 1
	v_cndmask_b32_e32 v32, v4, v32, vcc
	v_div_scale_f32 v4, s[6:7], v32, v32, 1.0
	v_rcp_f32_e32 v5, v4
	v_div_scale_f32 v6, vcc, 1.0, v32, 1.0
	v_fma_f32 v7, -v4, v5, 1.0
	v_fmac_f32_e32 v5, v7, v5
	v_mul_f32_e32 v7, v6, v5
	v_fma_f32 v8, -v4, v7, v6
	v_fmac_f32_e32 v7, v8, v5
	v_fma_f32 v4, -v4, v7, v6
	v_div_fmas_f32 v4, v4, v5, v7
	v_div_fixup_f32 v32, v4, v32, 1.0
	ds_write_b32 v31, v32
.Lprep_pq_skip:
	s_mov_b64 exec, -1
	v_mov_b32_e32 v201, v3
	v_mov_b32_e32 v199, v3
	s_cmp_eq_u32 s11, 1
	v_lshl_add_u64 v[10:11], s[22:23], 0, v[196:197]
	s_waitcnt vmcnt(0)
	v_lshl_add_u64 v[8:9], s[22:23], 0, v[200:201]
	v_lshl_add_u64 v[4:5], s[0:1], 0, v[2:3]
	s_cselect_b64 s[6:7], -1, 0
	s_cmp_lg_u32 s11, 1
	v_lshl_add_u64 v[6:7], s[0:1], 0, v[198:199]
	s_cbranch_scc1 .LBB0_992
	s_barrier

; __device__ __forceinline__ int launder_v(int v) { asm volatile("" : "+v"(v)); return v; }
; __device__ __forceinline__ float rsq_(float x) { return 1.0f / sqrtf(x); }
; #define PG8_STAGEB(bufoff, gbase) do { _Pragma("unroll") for (int _i = 0; _i < 2; ++_i) PG8_GL((const char*)(gbase) + voffB[_i], bufoff, _i); } while (0)
; #define PG8_STAGEA(bufoff, ubase, offs, h, kb) do { _Pragma("unroll") for (int _i = 0; _i < 2; ++_i) { \
;         if constexpr (P::GATHER) PG8_GL(S.A + (size_t)(kb) + (offs)[h][_i], bufoff, _i); \
;         else PG8_GL((const char*)(ubase) + (size_t)(h) * hstepA + (size_t)(kb) + voffA[_i], bufoff, _i); } } while (0)
; #define PG8_WAIT_V(n) asm volatile("s_waitcnt vmcnt(" #n ")" ::: "memory")
; #define PG8_BAR __builtin_amdgcn_s_barrier()
; __device__ __forceinline__ LAS float* T0(ldsp tab, int par) { return (LAS float*)(tab) + par * 256; }
; #define PROB_WS() unsigned char* w_ = ws; asm volatile("" : "+s"(w_))
; template <class P, bool ALIGN_EPI>
; __device__ __forceinline__ void gemm_phase(ldsp lds, ldsp tab, const P& S) {
;     ...
;     S.prepare(cur, 0, tab);
;     PG8_STAGEB(PG8_SB(0, 0), cB); PG8_STAGEB(PG8_SB(0, 1), cB + hstepB); PG8_STAGEA(PG8_SA(0, 0), cA, goc, 0, 0); PG8_STAGEA(PG8_SA(0, 1), cA, goc, 1, 0);
;     if (wr == 1) PG8_BAR;
;     PG8_WAIT_V(2); PG8_BAR;
;     PG8_STAGEB(PG8_SB(1, 0), cB + kstep); PG8_STAGEA(PG8_SA(1, 0), cA, goc, 0, kstep); PG8_STAGEB(PG8_SB(1, 1), cB + hstepB + kstep);
;     PG8_WAIT_V(6); PG8_BAR;
;     __device__ __forceinline__ void prepare(const Unit& u, int par, ldsp tab) const {
;         PROB_WS(); const float* ssql = (const float*)(w_ + WS_SSQL);
;         const int tid = launder_v(threadIdx.x); if (tid < 256) { const int row = u.pm * 256 + tid; const f32x4 a = gld4(ssql + (size_t)row * 8 + 4); T0(tab, par)[tid] = rsq_(((a[0] + a[1]) + (a[2] + a[3])) * (1.0f / 128.0f) + EPS); } }
.LBB0_1016:
	s_ashr_i32 s0, s2, 3
	s_add_i32 s0, s7, s0
	s_ashr_i32 s1, s0, 31
	s_lshr_b32 s1, s1, 27
	s_add_i32 s1, s0, s1
	s_ashr_i32 s2, s1, 5
	s_and_b32 s1, s1, 0xffe0
	s_sub_i32 s0, s0, s1
	s_bfe_i32 s1, s0, 0x80000
	s_bfe_u32 s1, s1, 0x3000c
	s_add_i32 s1, s0, s1
	s_lshl_b32 s6, s2, 3
	s_bfe_i32 s2, s1, 0x80000
	s_and_b32 s1, s1, 0xf8
	s_sub_i32 s0, s0, s1
	s_sext_i32_i8 s0, s0
	s_sext_i32_i16 s2, s2
	s_add_i32 s30, s6, s0
	s_mov_b64 s[0:1], s[4:5]
	v_mov_b32_e32 v1, v0
	s_movk_i32 s6, 0x100
	s_lshr_b32 s2, s2, 3
	s_nop 0
	v_cmp_gt_i32_e32 vcc, s6, v1
	s_and_saveexec_b64 s[6:7], vcc
	s_cbranch_execz .LBB0_1018
	s_waitcnt lgkmcnt(0)
	v_lshl_add_u32 v4, s30, 8, v1
	s_waitcnt lgkmcnt(0)
	v_ashrrev_i32_e32 v5, 31, v4
	v_lshlrev_b64 v[4:5], 5, v[4:5]
	v_lshl_add_u64 v[4:5], s[0:1], 0, v[4:5]
	v_add_co_u32_e32 v4, vcc, 0x464000, v4
	s_mov_b32 s0, 0xf800000
	s_nop 0
	v_addc_co_u32_e32 v5, vcc, 0, v5, vcc
	global_load_dwordx4 v[26:29], v[4:5], off offset:16
	v_lshl_add_u32 v31, v1, 2, 0
	v_add_u32_e32 v31, 0x20000, v31
.LBB0_1018:
	s_or_b64 exec, exec, s[6:7]
	s_add_u32 s49, s4, 0x250f4200
	s_waitcnt lgkmcnt(0)
	v_bfe_i32 v4, v16, 27, 1
	s_addc_u32 s50, s5, 0
	s_lshl_b32 s0, s26, 18
	v_lshlrev_b32_e32 v1, 4, v16
	v_lshrrev_b32_e32 v4, 22, v4
	s_add_u32 s0, s4, s0
	v_add_u32_e32 v4, v1, v4
	s_addc_u32 s1, s5, 0
	v_and_b32_e32 v4, 0xfffffc00, v4
	s_add_u32 s51, s0, 0x18f4000
	v_sub_u32_e32 v4, v1, v4
	s_addc_u32 s52, s1, 0
	s_ashr_i32 s31, s30, 31
	v_mov_b32_e32 v2, s2
	s_waitcnt lgkmcnt(0)
	v_lshrrev_b32_e32 v5, 4, v4
	s_ashr_i32 s15, s14, 31
	s_lshl_b64 s[0:1], s[30:31], 20
	v_readfirstlane_b32 s8, v2
	v_ashrrev_i32_e32 v2, 31, v16
	v_bitop3_b32 v4, v5, v4, 32 bitop3:0x6c
	s_add_u32 s38, s49, s0
	v_lshrrev_b32_e32 v2, 26, v2
	v_ashrrev_i32_e32 v6, 31, v4
	s_addc_u32 s39, s50, s1
	s_bfe_i64 s[0:1], s[8:9], 0x80000
	s_lshl_b64 s[6:7], s[14:15], 9
	v_add_u32_e32 v2, v16, v2
	v_lshrrev_b32_e32 v6, 26, v6
	s_mul_i32 s1, s6, s1
	s_mul_hi_u32 s8, s6, s0
	s_lshr_b64 s[10:11], s[14:15], 23
	v_ashrrev_i32_e32 v2, 6, v2
	v_add_u32_e32 v6, v4, v6
	s_add_i32 s1, s8, s1
	s_mul_i32 s8, s10, s0
	v_lshlrev_b32_e32 v5, 3, v2
	v_ashrrev_i32_e32 v7, 6, v6
	v_and_b32_e32 v6, 0xc0, v6
	s_add_i32 s1, s1, s8
	s_mul_i32 s0, s6, s0
	v_and_b32_e32 v5, -16, v5
	v_lshlrev_b32_e32 v2, 5, v2
	v_sub_u32_e32 v4, v4, v6
	s_add_u32 s40, s51, s0
	v_add_u32_e32 v5, v7, v5
	v_and_b32_e32 v2, 32, v2
	v_ashrrev_i16_sdwa v4, v248, sext(v4) dst_sel:DWORD dst_unused:UNUSED_PAD src0_sel:DWORD src1_sel:BYTE_0
	s_addc_u32 s41, s52, s1
	v_add_u32_sdwa v4, v2, sext(v4) dst_sel:DWORD dst_unused:UNUSED_PAD src0_sel:DWORD src1_sel:WORD_0
	v_lshlrev_b32_e32 v2, 1, v5
	v_lshrrev_b32_e32 v6, 2, v5
	v_and_b32_e32 v7, 3, v7
	s_mov_b32 s1, 0x7fffffe0
	v_and_b32_e32 v2, 24, v2
	v_and_b32_e32 v6, 4, v6
	v_and_or_b32 v7, v5, s1, v7
	v_or3_b32 v6, v7, v6, v2
	v_lshlrev_b32_e32 v2, 12, v5
	v_mul_lo_u32 v5, v6, s14
	v_add_u32_e32 v1, 0x2000, v1
	v_lshl_add_u32 v2, v4, 1, v2
	v_add_lshl_u32 v132, v5, v4, 1
	v_ashrrev_i32_e32 v4, 31, v1
	v_lshrrev_b32_e32 v4, 22, v4
	v_add_u32_e32 v4, v1, v4
	v_ashrrev_i32_e32 v4, 10, v4
	v_mul_i32_i24_e32 v5, 0x400, v4
	v_sub_u32_e32 v1, v1, v5
	v_lshrrev_b32_e32 v5, 4, v1
	v_bitop3_b32 v1, v5, v1, 32 bitop3:0x6c
	v_ashrrev_i32_e32 v6, 31, v1
	v_lshrrev_b32_e32 v6, 26, v6
	v_lshlrev_b32_e32 v5, 3, v4
	v_add_u32_e32 v6, v1, v6
	v_and_b32_e32 v5, -16, v5
	v_ashrrev_i32_e32 v7, 6, v6
	v_and_b32_e32 v6, 0xc0, v6
	v_add_u32_e32 v5, v7, v5
	v_lshlrev_b32_e32 v4, 5, v4
	v_sub_u32_e32 v1, v1, v6
	v_and_b32_e32 v7, 3, v7
	v_and_b32_e32 v4, 32, v4
	v_ashrrev_i16_sdwa v1, v248, sext(v1) dst_sel:DWORD dst_unused:UNUSED_PAD src0_sel:DWORD src1_sel:BYTE_0
	v_and_or_b32 v7, v5, s1, v7
	s_ashr_i32 s1, s3, 6
	v_add_u32_sdwa v1, v4, sext(v1) dst_sel:DWORD dst_unused:UNUSED_PAD src0_sel:DWORD src1_sel:WORD_0
	v_lshlrev_b32_e32 v4, 1, v5
	v_lshrrev_b32_e32 v6, 2, v5
	s_lshl_b32 s8, s1, 10
	v_and_b32_e32 v4, 24, v4
	v_and_b32_e32 v6, 4, v6
	s_add_i32 s53, s8, 0
	v_or3_b32 v4, v7, v6, v4
	s_add_i32 m0, s53, 0x10000
	s_ashr_i32 s0, s3, 8
	v_mul_lo_u32 v4, v4, s14
	s_lshl_b64 s[10:11], s[14:15], 8
	global_load_lds_dwordx4 v132, s[40:41]
	s_add_i32 m0, s53, 0x12000
	v_add_lshl_u32 v136, v4, v1, 1
	s_add_u32 s12, s40, s10
	global_load_lds_dwordx4 v136, s[40:41]
	s_addc_u32 s13, s41, s11
	s_add_i32 m0, s53, 0x14000
	v_mov_b32_e32 v133, v3
	v_mov_b32_e32 v137, v3
	global_load_lds_dwordx4 v132, s[12:13]
	s_add_i32 m0, s53, 0x16000
	s_add_i32 s54, s53, 0x2000
	v_lshlrev_b32_e32 v5, 12, v5
	v_lshl_add_u64 v[8:9], s[12:13], 0, v[132:133]
	v_lshl_add_u64 v[10:11], s[12:13], 0, v[136:137]
	global_load_lds_dwordx4 v136, s[12:13]
	s_mov_b32 m0, s53
	s_add_u32 s12, s38, 0x80000
	v_lshl_add_u32 v134, v1, 1, v5
	global_load_lds_dwordx4 v2, s[38:39]
	s_mov_b32 m0, s54
	s_addc_u32 s13, s39, 0
	s_add_i32 s55, s53, 0x4000
	global_load_lds_dwordx4 v134, s[38:39]
	s_mov_b32 m0, s55
	s_add_i32 s56, s53, 0x6000
	global_load_lds_dwordx4 v2, s[12:13]
	s_mov_b32 m0, s56
	v_mov_b32_e32 v135, v3
	global_load_lds_dwordx4 v134, s[12:13]
	v_cmp_gt_i32_e32 vcc, 0x100, v0
	s_and_b64 exec, exec, vcc
	s_cbranch_execz .Lprep_pkv_skip
	s_waitcnt vmcnt(8)
	v_mov_b32_e32 v34, v27
	v_mov_b32_e32 v35, v28
	v_mov_b32_e32 v4, v26
	v_mov_b32_e32 v5, v29
	v_pk_add_f32 v[4:5], v[34:35], v[4:5]
	s_nop 0
	v_add_f32_e32 v32, v4, v5
	v_fmamk_f32 v32, v32, 0x3c000000, v247
	v_mul_f32_e32 v4, 0x4f800000, v32
	v_cmp_gt_f32_e32 vcc, 0xf800000, v32
	s_nop 1
	v_cndmask_b32_e32 v32, v32, v4, vcc
	v_sqrt_f32_e32 v4, v32
	s_nop 0
	v_add_u32_e32 v5, -1, v4
	v_add_u32_e32 v6, 1, v4
	v_fma_f32 v7, -v5, v4, v32
	v_fma_f32 v33, -v6, v4, v32
	v_cmp_ge_f32_e64 s[12:13], 0, v7
	s_nop 1
	v_cndmask_b32_e64 v4, v4, v5, s[12:13]
	v_cmp_lt_f32_e64 s[12:13], 0, v33
	s_nop 1
	v_cndmask_b32_e64 v4, v4, v6, s[12:13]
	v_mul_f32_e32 v5, 0x37800000, v4
	v_cndmask_b32_e32 v4, v4, v5, vcc
	v_cmp_class_f32_e32 vcc, v32, v242
	s_nop 1
	v_cndmask_b32_e32 v32, v4, v32, vcc
	v_div_scale_f32 v4, s[12:13], v32, v32, 1.0
	v_rcp_f32_e32 v5, v4
	v_div_scale_f32 v6, vcc, 1.0, v32, 1.0
	v_fma_f32 v7, -v4, v5, 1.0
	v_fmac_f32_e32 v5, v7, v5
	v_mul_f32_e32 v7, v6, v5
	v_fma_f32 v33, -v4, v7, v6
	v_fmac_f32_e32 v7, v33, v5
	v_fma_f32 v4, -v4, v7, v6
	v_div_fmas_f32 v4, v4, v5, v7
	v_div_fixup_f32 v32, v4, v32, 1.0
	ds_write_b32 v31, v32
.Lprep_pkv_skip:
	s_mov_b64 exec, -1
	s_cmp_eq_u32 s0, 1
	v_lshl_add_u64 v[4:5], s[40:41], 0, v[132:133]
	v_lshl_add_u64 v[6:7], s[40:41], 0, v[136:137]
	v_lshl_add_u64 v[12:13], s[38:39], 0, v[2:3]
	v_lshl_add_u64 v[14:15], s[38:39], 0, v[134:135]
	s_cselect_b64 s[12:13], -1, 0
	s_cmp_lg_u32 s0, 1
	s_cbranch_scc1 .LBB0_1020
	s_barrier

; __device__ __forceinline__ int launder_v(int v) { asm volatile("" : "+v"(v)); return v; }
; __device__ __forceinline__ float rsq_(float x) { return 1.0f / sqrtf(x); }
; __device__ __forceinline__ LAS float* T0(ldsp tab, int par) { return (LAS float*)(tab) + par * 256; }
; __device__ __forceinline__ LAS float* T3(ldsp tab, int par) { return (LAS float*)(tab + 6144) + par * 512; }
; #define PROB_WS() unsigned char* w_ = ws; asm volatile("" : "+s"(w_))
;     __device__ __forceinline__ void prepare(const Unit& u, int par, ldsp tab) const {
;         PROB_WS(); const float* ssqx = (const float*)(w_ + WS_SSQX);
;         const int tid = launder_v(threadIdx.x); if (tid < 256) { const int row = u.pm * 256 + tid; const float bvl = ((const float*)(w_ + WS_BGU))[((size_t)i * 2 + (u.pm >> 5)) * (2 * DFF) + u.pn * 256 + tid];
;             T0(tab, par)[tid] = rsq_(sum16(ssqx + (size_t)row * 16) * (1.0f / 1024.0f) + EPS); T3(tab, par)[tid] = bvl; } }
.LBB0_1908:
	v_readlane_b32 s0, v253, 5
	v_readlane_b32 s1, v253, 6
	s_cmp_le_i32 s0, s59
	s_cselect_b64 s[0:1], -1, 0
	s_and_b64 s[0:1], s[0:1], s[10:11]
	s_andn2_b64 vcc, exec, s[0:1]
	s_cbranch_vccnz .LBB0_1929
	v_readlane_b32 s0, v253, 7
	v_readlane_b32 s2, v253, 9
	v_readlane_b32 s3, v253, 10
	s_mov_b64 s[4:5], s[2:3]
	v_readlane_b32 s40, v253, 3
	v_mov_b32_e32 v12, v0
	s_cmpk_gt_i32 s40, 0x4ff
	v_readfirstlane_b32 s3, v12
	v_readlane_b32 s1, v253, 8
	s_cbranch_scc1 .LBB0_1929
	s_ashr_i32 s41, s40, 31
	s_lshr_b32 s0, s41, 29
	s_add_i32 s0, s40, s0
	s_ashr_i32 s1, s0, 3
	s_and_b32 s0, s0, -8
	s_sub_i32 s0, s40, s0
	s_cmp_lt_i32 s0, 0
	s_movk_i32 s2, 0xa1
	s_cselect_b32 s2, s2, 0xa0
	s_mul_i32 s0, s0, s2
	s_add_i32 s0, s0, s1
	s_mul_hi_i32 s1, s0, 0x66666667
	s_lshr_b32 s2, s1, 31
	s_ashr_i32 s1, s1, 6
	s_add_i32 s1, s1, s2
	s_lshl_b32 s2, s1, 3
	s_mulk_i32 s1, 0xa0
	s_sub_i32 s0, s0, s1
	s_bfe_u32 s1, s0, 0x3001c
	s_add_i32 s1, s0, s1
	s_sext_i32_i16 s6, s1
	s_and_b32 s1, s1, 0xfff8
	s_sub_i32 s0, s0, s1
	s_sext_i32_i16 s0, s0
	s_lshr_b32 s10, s6, 3
	s_add_i32 s20, s2, s0
	s_ashr_i32 s2, s6, 3
	s_mov_b64 s[0:1], s[4:5]
	s_waitcnt lgkmcnt(0)
	v_mov_b32_e32 v4, v0
	s_movk_i32 s6, 0x100
	s_nop 0
	v_cmp_gt_i32_e32 vcc, s6, v4
	s_and_saveexec_b64 s[6:7], vcc
	v_readlane_b32 s14, v255, 34
	v_readlane_b32 s15, v255, 35
	s_cbranch_execz .LBB0_1912
	s_ashr_i32 s8, s20, 5
	s_ashr_i32 s11, s8, 31
	s_add_u32 s8, s8, s14
	s_addc_u32 s11, s11, 0
	s_lshl_b32 s12, s2, 8
	s_mulk_i32 s11, 0x5000
	s_mul_hi_u32 s14, s8, 0x5000
	s_ashr_i32 s13, s12, 31
	s_add_i32 s14, s14, s11
	s_mulk_i32 s8, 0x5000
	s_add_u32 s8, s0, s8
	s_addc_u32 s11, s1, s14
	s_lshl_b64 s[12:13], s[12:13], 2
	v_lshl_add_u32 v6, s20, 8, v4
	s_add_u32 s12, s8, s12
	v_ashrrev_i32_e32 v5, 31, v4
	s_addc_u32 s13, s11, s13
	v_ashrrev_i32_e32 v7, 31, v6
	s_waitcnt vmcnt(0)
	v_lshl_add_u64 v[8:9], v[4:5], 2, s[12:13]
	s_mov_b32 s8, 0x270000
	v_lshlrev_b64 v[6:7], 6, v[6:7]
	v_add_co_u32_e32 v8, vcc, s8, v8
	v_lshl_add_u64 v[6:7], s[0:1], 0, v[6:7]
	s_mov_b64 s[0:1], 0x364000
	v_addc_co_u32_e32 v9, vcc, 0, v9, vcc
	v_lshl_add_u64 v[10:11], v[6:7], 0, s[0:1]
	s_mov_b32 s0, 0x364000
	v_add_co_u32_e32 v6, vcc, s0, v6
	flat_load_dword v30, v[8:9]
	s_nop 0
	v_addc_co_u32_e32 v7, vcc, 0, v7, vcc
	global_load_dwordx4 v[26:29], v[6:7], off
	s_nop 0
	global_load_dwordx4 v[14:17], v[10:11], off offset:48
	global_load_dwordx4 v[18:21], v[10:11], off offset:32
	global_load_dwordx4 v[22:25], v[10:11], off offset:16
	s_mov_b32 s0, 0xf800000
	v_lshl_add_u32 v31, v4, 2, 0
; __device__ __forceinline__ int launder_v(int v) { asm volatile("" : "+v"(v)); return v; }
; __device__ __forceinline__ float rsq_(float x) { return 1.0f / sqrtf(x); }
; #define PG8_STAGEB(bufoff, gbase) do { _Pragma("unroll") for (int _i = 0; _i < 2; ++_i) PG8_GL((const char*)(gbase) + voffB[_i], bufoff, _i); } while (0)
; #define PG8_STAGEA(bufoff, ubase, offs, h, kb) do { _Pragma("unroll") for (int _i = 0; _i < 2; ++_i) { \
;         if constexpr (P::GATHER) PG8_GL(S.A + (size_t)(kb) + (offs)[h][_i], bufoff, _i); \
;         else PG8_GL((const char*)(ubase) + (size_t)(h) * hstepA + (size_t)(kb) + voffA[_i], bufoff, _i); } } while (0)
; #define PG8_WAIT_V(n) asm volatile("s_waitcnt vmcnt(" #n ")" ::: "memory")
; #define PG8_BAR __builtin_amdgcn_s_barrier()
; __device__ __forceinline__ LAS float* T0(ldsp tab, int par) { return (LAS float*)(tab) + par * 256; }
; __device__ __forceinline__ LAS float* T3(ldsp tab, int par) { return (LAS float*)(tab + 6144) + par * 512; }
; #define PROB_WS() unsigned char* w_ = ws; asm volatile("" : "+s"(w_))
; template <class P, bool ALIGN_EPI>
; __device__ __forceinline__ void gemm_phase(ldsp lds, ldsp tab, const P& S) {
;     ...
;     S.prepare(cur, 0, tab);
;     PG8_STAGEB(PG8_SB(0, 0), cB); PG8_STAGEB(PG8_SB(0, 1), cB + hstepB); PG8_STAGEA(PG8_SA(0, 0), cA, goc, 0, 0); PG8_STAGEA(PG8_SA(0, 1), cA, goc, 1, 0);
;     if (wr == 1) PG8_BAR;
;     PG8_WAIT_V(2); PG8_BAR;
;     PG8_STAGEB(PG8_SB(1, 0), cB + kstep); PG8_STAGEA(PG8_SA(1, 0), cA, goc, 0, kstep); PG8_STAGEB(PG8_SB(1, 1), cB + hstepB + kstep);
;     PG8_WAIT_V(6); PG8_BAR;
;     __device__ __forceinline__ void prepare(const Unit& u, int par, ldsp tab) const {
;         PROB_WS(); const float* ssqx = (const float*)(w_ + WS_SSQX);
;         const int tid = launder_v(threadIdx.x); if (tid < 256) { const int row = u.pm * 256 + tid; const float bvl = ((const float*)(w_ + WS_BGU))[((size_t)i * 2 + (u.pm >> 5)) * (2 * DFF) + u.pn * 256 + tid];
;             T0(tab, par)[tid] = rsq_(sum16(ssqx + (size_t)row * 16) * (1.0f / 1024.0f) + EPS); T3(tab, par)[tid] = bvl; } }
.LBB0_1912:
	s_or_b64 exec, exec, s[6:7]
	v_bfe_i32 v4, v12, 27, 1
	v_lshlrev_b32_e32 v1, 4, v12
	v_lshrrev_b32_e32 v4, 22, v4
	s_mul_i32 s8, s58, 0x500000
	s_add_u32 s42, s4, 0x1f0f4000
	v_add_u32_e32 v4, v1, v4
	s_addc_u32 s43, s5, 0
	s_lshl_b64 s[0:1], s[8:9], 1
	v_and_b32_e32 v4, 0xfffffc00, v4
	s_add_u32 s0, s4, s0
	v_sub_u32_e32 v4, v1, v4
	s_addc_u32 s1, s5, s1
	v_ashrrev_i32_e32 v2, 31, v12
	v_lshrrev_b32_e32 v5, 4, v4
	s_add_u32 s8, s0, 0x22f4000
	v_lshrrev_b32_e32 v2, 26, v2
	v_bitop3_b32 v4, v5, v4, 32 bitop3:0x6c
	s_addc_u32 s44, s1, 0
	s_ashr_i32 s21, s20, 31
	v_add_u32_e32 v2, v12, v2
	v_ashrrev_i32_e32 v6, 31, v4
	s_lshl_b64 s[0:1], s[20:21], 19
	v_ashrrev_i32_e32 v2, 6, v2
	v_lshrrev_b32_e32 v6, 26, v6
	s_add_u32 s0, s42, s0
	s_sext_i32_i16 s6, s10
	v_lshlrev_b32_e32 v5, 3, v2
	v_add_u32_e32 v6, v4, v6
	s_addc_u32 s1, s43, s1
	s_ashr_i32 s7, s6, 31
	v_and_b32_e32 v5, -16, v5
	v_ashrrev_i32_e32 v7, 6, v6
	v_and_b32_e32 v6, 0xc0, v6
	s_lshl_b64 s[6:7], s[6:7], 19
	v_add_u32_e32 v5, v7, v5
	v_sub_u32_e32 v4, v4, v6
	s_add_u32 s22, s8, s6
	v_lshlrev_b32_e32 v2, 5, v2
	v_ashrrev_i16_sdwa v4, v248, sext(v4) dst_sel:DWORD dst_unused:UNUSED_PAD src0_sel:DWORD src1_sel:BYTE_0
	v_lshlrev_b32_e32 v6, 1, v5
	v_lshrrev_b32_e32 v8, 2, v5
	v_and_b32_e32 v7, 3, v7
	s_mov_b32 s6, 0x1fffe0
	v_and_b32_e32 v2, 32, v2
	v_bfe_i32 v4, v4, 0, 16
	v_and_b32_e32 v6, 24, v6
	v_and_b32_e32 v8, 4, v8
	v_and_or_b32 v7, v5, s6, v7
	v_or3_b32 v6, v7, v8, v6
	v_add_lshl_u32 v4, v2, v4, 1
	v_add_u32_e32 v1, 0x2000, v1
	v_lshl_add_u32 v2, v5, 11, v4
	v_lshl_add_u32 v148, v6, 11, v4
	v_ashrrev_i32_e32 v4, 31, v1
	v_lshrrev_b32_e32 v4, 22, v4
	v_add_u32_e32 v4, v1, v4
	v_ashrrev_i32_e32 v4, 10, v4
	v_mul_i32_i24_e32 v5, 0x400, v4
	v_sub_u32_e32 v1, v1, v5
	v_lshrrev_b32_e32 v5, 4, v1
	v_bitop3_b32 v1, v5, v1, 32 bitop3:0x6c
	v_ashrrev_i32_e32 v6, 31, v1
	v_lshrrev_b32_e32 v6, 26, v6
	v_lshlrev_b32_e32 v5, 3, v4
	v_add_u32_e32 v6, v1, v6
	s_addc_u32 s23, s44, s7
	v_and_b32_e32 v5, -16, v5
	v_ashrrev_i32_e32 v7, 6, v6
	v_and_b32_e32 v6, 0xc0, v6
	s_ashr_i32 s11, s3, 6
	v_add_u32_e32 v5, v7, v5
	v_sub_u32_e32 v1, v1, v6
	s_lshl_b32 s45, s11, 10
	v_lshlrev_b32_e32 v4, 5, v4
	v_ashrrev_i16_sdwa v1, v248, sext(v1) dst_sel:DWORD dst_unused:UNUSED_PAD src0_sel:DWORD src1_sel:BYTE_0
	v_lshlrev_b32_e32 v6, 1, v5
	v_lshrrev_b32_e32 v8, 2, v5
	v_and_b32_e32 v7, 3, v7
	s_add_i32 s48, s45, 0
	v_and_b32_e32 v4, 32, v4
	v_bfe_i32 v1, v1, 0, 16
	v_and_b32_e32 v6, 24, v6
	v_and_b32_e32 v8, 4, v8
	v_and_or_b32 v7, v5, s6, v7
	s_add_i32 m0, s48, 0x10000
	s_ashr_i32 s10, s3, 8
	v_or3_b32 v6, v7, v8, v6
	v_add_lshl_u32 v1, v4, v1, 1
	global_load_lds_dwordx4 v148, s[22:23]
	s_add_i32 m0, s48, 0x12000
	v_lshl_add_u32 v152, v6, 11, v1
	s_add_u32 s6, s22, 0x40000
	global_load_lds_dwordx4 v152, s[22:23]
	s_addc_u32 s7, s23, 0
	s_add_i32 m0, s48, 0x14000
	s_add_i32 s49, s48, 0x2000
	global_load_lds_dwordx4 v148, s[6:7]
	s_add_i32 m0, s48, 0x16000
	v_lshl_add_u32 v150, v5, 11, v1
	global_load_lds_dwordx4 v152, s[6:7]
	s_mov_b32 m0, s48
	s_add_u32 s6, s0, 0x40000
	global_load_lds_dwordx4 v2, s[0:1]
	s_mov_b32 m0, s49
	s_addc_u32 s7, s1, 0
	s_add_i32 s50, s48, 0x4000
	global_load_lds_dwordx4 v150, s[0:1]
	s_mov_b32 m0, s50
	s_add_i32 s51, s48, 0x6000
	global_load_lds_dwordx4 v2, s[6:7]
	s_mov_b32 m0, s51
	v_mov_b32_e32 v149, v3
	global_load_lds_dwordx4 v150, s[6:7]
	v_cmp_gt_i32_e32 vcc, 0x100, v0
	s_and_b64 exec, exec, vcc
	s_cbranch_execz .Lprep_pgu_skip
	s_waitcnt vmcnt(8)
	v_add_f32_e32 v32, v26, v27
	v_add_f32_e32 v5, v28, v29
	v_add_f32_e32 v32, v32, v5
	v_add_f32_e32 v5, v22, v23
	v_add_f32_e32 v6, v24, v25
	v_add_f32_e32 v5, v5, v6
	v_add_f32_e32 v32, v32, v5
	v_add_f32_e32 v5, v18, v19
	v_add_f32_e32 v6, v20, v21
	v_add_f32_e32 v5, v5, v6
	v_add_f32_e32 v32, v32, v5
	v_add_f32_e32 v5, v14, v15
	v_add_f32_e32 v6, v16, v17
	v_add_f32_e32 v5, v5, v6
	v_add_f32_e32 v32, v32, v5
	v_fmamk_f32 v32, v32, 0x3a800000, v247
	v_cmp_gt_f32_e32 vcc, 0xf800000, v32
	v_mul_f32_e32 v5, 0x4f800000, v32
	s_nop 0
	v_cndmask_b32_e32 v32, v32, v5, vcc
	v_sqrt_f32_e32 v5, v32
	s_nop 0
	v_add_u32_e32 v6, -1, v5
	v_fma_f32 v7, -v6, v5, v32
	v_cmp_ge_f32_e64 s[6:7], 0, v7
	v_add_u32_e32 v7, 1, v5
	s_nop 0
	v_cndmask_b32_e64 v6, v5, v6, s[6:7]
	v_fma_f32 v5, -v7, v5, v32
	v_cmp_lt_f32_e64 s[6:7], 0, v5
	s_nop 1
	v_cndmask_b32_e64 v5, v6, v7, s[6:7]
	v_mul_f32_e32 v6, 0x37800000, v5
	v_cndmask_b32_e32 v5, v5, v6, vcc
	v_cmp_class_f32_e32 vcc, v32, v242
	s_nop 1
	v_cndmask_b32_e32 v32, v5, v32, vcc
	v_div_scale_f32 v5, s[6:7], v32, v32, 1.0
	v_rcp_f32_e32 v6, v5
	s_nop 0
	v_fma_f32 v7, -v5, v6, 1.0
	v_fmac_f32_e32 v6, v7, v6
	v_div_scale_f32 v7, vcc, 1.0, v32, 1.0
	v_mul_f32_e32 v8, v7, v6
	v_fma_f32 v9, -v5, v8, v7
	v_fmac_f32_e32 v8, v9, v6
	v_fma_f32 v5, -v5, v8, v7
	v_div_fmas_f32 v5, v5, v6, v8
	v_div_fixup_f32 v32, v5, v32, 1.0
	v_add_u32_e32 v5, 0x20000, v31
	ds_write_b32 v5, v32
	v_add_u32_e32 v32, 0x21800, v31
	s_waitcnt lgkmcnt(0)
	ds_write_b32 v32, v30
.Lprep_pgu_skip:
	s_mov_b64 exec, -1
	v_mov_b32_e32 v153, v3
	v_mov_b32_e32 v151, v3
	s_cmp_eq_u32 s10, 1
	v_lshl_add_u64 v[10:11], s[22:23], 0, v[148:149]
	s_waitcnt vmcnt(0)
	v_lshl_add_u64 v[8:9], s[22:23], 0, v[152:153]
	v_lshl_add_u64 v[4:5], s[0:1], 0, v[2:3]
	s_cselect_b64 s[6:7], -1, 0
	s_cmp_lg_u32 s10, 1
	v_lshl_add_u64 v[6:7], s[0:1], 0, v[150:151]
	s_cbranch_scc1 .LBB0_1914
	s_barrier
